# LN1+router setup: 128 router-weight loads per wave issued as 8 pipelined chunks (3 in flight) instead of 16 serial load-wait batches
# speedup vs baseline: 1.0062x; 1.0062x over previous
; #define LAS __attribute__((address_space(3)))
; template <bool RES_F32> ...
;     const int wid = __builtin_amdgcn_readfirstlane(tid >> 6), lane = tid & 63;
;     float ALPHA = 1.4142135623730951f; asm volatile("" : "+v"(ALPHA));
;     LAS float* xs = (LAS float*)lds; LAS float* part = (LAS float*)(lds + LNR_PART); LAS float* scs = (LAS float*)(lds + LNR_SC); LAS float* sels = (LAS float*)(lds + LNR_SEL);
;     LAS int* ble = (LAS int*)(lds + LNR_BLE); LAS int* hist = (LAS int*)(lds + LNR_HIST);
;     f16x8 bw[8][2];
;     { const float* rwp = rw + (size_t)(256 * wid + 8 * (lane >> 4)) * 32 + (lane & 15);
; #pragma unroll
;       for (int ks = 0; ks < 8; ++ks)
; #pragma unroll
;         for (int hf = 0; hf < 2; ++hf)
; #pragma unroll
;           for (int j = 0; j < 8; ++j) bw[ks][hf][j] = (_Float16)rwp[(32 * ks + j) * 32 + 16 * hf]; }
;     typedef typename std::conditional<RES_F32, f32x4, u32x2>::type res_t;
;     typedef typename std::conditional<F8_MIX != 0, unsigned, u32x2>::type mix_t;
;     mix_t mv[2][8]; res_t rv[2][8];
;     ...
;     const int ntile = T_ / 16;
;     int ntl = 0;
;     if (bid < ntile) LNR_LOAD(bid, 0);
.LBB0_767:
	s_andn2_b64 vcc, exec, s[0:1]
	s_cbranch_vccnz .LBB0_901
	s_mov_b64 s[64:65], s[76:77]
	s_load_dwordx4 s[68:71], s[64:65], 0xe0
	s_waitcnt lgkmcnt(0)
	s_add_u32 s54, s70, 0x1c600000
	s_addc_u32 s55, s71, 0
	s_add_u32 s96, s70, 0x24600000
	s_addc_u32 s97, s71, 0
	s_add_u32 s66, s70, 0x100000
	s_addc_u32 s67, s71, 0
	s_add_u32 s92, s70, 0x900000
	s_addc_u32 s93, s71, 0
	s_add_u32 s52, s70, 0x940000
	s_addc_u32 s53, s71, 0
	s_add_u32 s34, s70, 0x980000
	s_addc_u32 s35, s71, 0
	s_lshl_b32 s36, s33, 6
	s_lshl_b64 s[0:1], s[36:37], 2
	s_add_u32 s24, s70, s0
	s_addc_u32 s25, s71, s1
	v_readlane_b32 s0, v255, 55
	v_readlane_b32 s1, v255, 56
	s_andn2_b64 vcc, exec, s[0:1]
	s_mov_b64 s[0:1], -1
	s_cbranch_vccnz .LBB0_807
	v_readlane_b32 s2, v253, 26
	v_mbcnt_lo_u32_b32 v64, -1, 0
	v_mbcnt_hi_u32_b32 v64, -1, v64
	v_readlane_b32 s3, v253, 27
	s_waitcnt vmcnt(0)
	v_add_u32_e32 v80, s5, v64
	v_mov_b32_e32 v82, 0x3fb504f3
	v_readfirstlane_b32 s0, v80
	s_mov_b32 s56, 0
	s_and_b64 vcc, exec, s[2:3]
	s_cbranch_vccz .LBB0_776
	s_load_dwordx4 s[72:75], s[64:65], 0xa8
	s_load_dwordx4 s[40:43], s[64:65], 0x8
	v_lshrrev_b32_e32 v0, 1, v64
	s_ashr_i32 s0, s0, 6
	v_and_b32_e32 v0, 24, v0
	v_lshl_or_b32 v0, s0, 8, v0
	v_ashrrev_i32_e32 v1, 31, v0
	v_lshlrev_b64 v[0:1], 7, v[0:1]
	v_and_b32_e32 v2, 15, v64
	s_waitcnt lgkmcnt(0)
	v_lshl_add_u64 v[0:1], s[40:41], 0, v[0:1]
	v_lshlrev_b32_e32 v232, 2, v2
	v_lshl_add_u64 v[56:57], v[0:1], 0, v[232:233]
	s_add_u32 s76, s70, 0x36600000
	s_addc_u32 s77, s71, 0
	s_lshl_b32 s78, s0, 1
	s_ashr_i32 s79, s78, 31
	s_lshl_b64 s[84:85], s[78:79], 11
	v_readlane_b32 s2, v253, 44
	v_readlane_b32 s3, v253, 45
	v_and_b32_e32 v81, 63, v64
	v_mov_b32_e32 v83, v82
	v_mov_b32_e32 v100, v82
	v_mov_b32_e32 v101, v82
	v_cmp_gt_i32_e64 s[38:39], 16, v80
	s_add_u32 s1, s84, s2
	s_addc_u32 s2, s85, s3
	s_or_b32 s60, s78, 1
	s_ashr_i32 s61, s60, 31
	v_mov_b32_e32 v67, s2
	v_readlane_b32 s2, v254, 55
	v_add_co_u32_e32 v138, vcc, 0x2000, v56
	s_nop 1
	v_addc_co_u32_e32 v139, vcc, 0, v57, vcc
	v_add_co_u32_e32 v140, vcc, 0x4000, v56
	s_nop 1
	v_addc_co_u32_e32 v141, vcc, 0, v57, vcc
	v_add_co_u32_e32 v142, vcc, 0x6000, v56
	s_nop 1
	v_addc_co_u32_e32 v143, vcc, 0, v57, vcc
	v_add_co_u32_e32 v144, vcc, 0x8000, v56
	s_nop 1
	v_addc_co_u32_e32 v145, vcc, 0, v57, vcc
	global_load_dword v0, v[56:57], off
	global_load_dword v65, v[56:57], off offset:128
	global_load_dword v1, v[56:57], off offset:256
	global_load_dword v66, v[56:57], off offset:384
	global_load_dword v2, v[56:57], off offset:512
	global_load_dword v68, v[56:57], off offset:640
	global_load_dword v3, v[56:57], off offset:768
	global_load_dword v69, v[56:57], off offset:896
	global_load_dword v4, v[56:57], off offset:64
	global_load_dword v70, v[56:57], off offset:192
	global_load_dword v5, v[56:57], off offset:320
	global_load_dword v71, v[56:57], off offset:448
	global_load_dword v6, v[56:57], off offset:576
	global_load_dword v72, v[56:57], off offset:704
	global_load_dword v7, v[56:57], off offset:832
	global_load_dword v73, v[56:57], off offset:960
	global_load_dword v8, v[138:139], off offset:-4096
	global_load_dword v74, v[138:139], off offset:-3968
	global_load_dword v9, v[138:139], off offset:-3840
	global_load_dword v75, v[138:139], off offset:-3712
	global_load_dword v10, v[138:139], off offset:-3584
	global_load_dword v76, v[138:139], off offset:-3456
	global_load_dword v11, v[138:139], off offset:-3328
	global_load_dword v77, v[138:139], off offset:-3200
	global_load_dword v12, v[138:139], off offset:-4032
	global_load_dword v78, v[138:139], off offset:-3904
	global_load_dword v13, v[138:139], off offset:-3776
	global_load_dword v79, v[138:139], off offset:-3648
	global_load_dword v14, v[138:139], off offset:-3520
	global_load_dword v84, v[138:139], off offset:-3392
	global_load_dword v15, v[138:139], off offset:-3264
	global_load_dword v85, v[138:139], off offset:-3136
	global_load_dword v16, v[138:139], off
	global_load_dword v86, v[138:139], off offset:128
	global_load_dword v17, v[138:139], off offset:256
	global_load_dword v87, v[138:139], off offset:384
	global_load_dword v18, v[138:139], off offset:512
	global_load_dword v88, v[138:139], off offset:640
	global_load_dword v19, v[138:139], off offset:768
	global_load_dword v89, v[138:139], off offset:896
	global_load_dword v20, v[138:139], off offset:64
	global_load_dword v90, v[138:139], off offset:192
	global_load_dword v21, v[138:139], off offset:320
	global_load_dword v91, v[138:139], off offset:448
	global_load_dword v22, v[138:139], off offset:576
	global_load_dword v92, v[138:139], off offset:704
	global_load_dword v23, v[138:139], off offset:832
	global_load_dword v93, v[138:139], off offset:960
	s_waitcnt vmcnt(32)
	v_cvt_pk_f16_f32 v0, v0, v65
	v_cvt_pk_f16_f32 v1, v1, v66
	v_cvt_pk_f16_f32 v2, v2, v68
	v_cvt_pk_f16_f32 v3, v3, v69
	v_cvt_pk_f16_f32 v4, v4, v70
	v_cvt_pk_f16_f32 v5, v5, v71
	v_cvt_pk_f16_f32 v6, v6, v72
	v_cvt_pk_f16_f32 v7, v7, v73
	global_load_dword v24, v[140:141], off offset:-4096
	global_load_dword v94, v[140:141], off offset:-3968
	global_load_dword v25, v[140:141], off offset:-3840
	global_load_dword v95, v[140:141], off offset:-3712
	global_load_dword v26, v[140:141], off offset:-3584
	global_load_dword v96, v[140:141], off offset:-3456
	global_load_dword v27, v[140:141], off offset:-3328
	global_load_dword v97, v[140:141], off offset:-3200
	global_load_dword v28, v[140:141], off offset:-4032
	global_load_dword v98, v[140:141], off offset:-3904
	global_load_dword v29, v[140:141], off offset:-3776
	global_load_dword v99, v[140:141], off offset:-3648
	global_load_dword v30, v[140:141], off offset:-3520
	global_load_dword v102, v[140:141], off offset:-3392
	global_load_dword v31, v[140:141], off offset:-3264
	global_load_dword v103, v[140:141], off offset:-3136
	s_waitcnt vmcnt(32)
; template <bool RES_F32> ...
;     ...
;     { const float* rwp = rw + (size_t)(256 * wid + 8 * (lane >> 4)) * 32 + (lane & 15);
; #pragma unroll
;       for (int ks = 0; ks < 8; ++ks)
; #pragma unroll
;         for (int hf = 0; hf < 2; ++hf)
; #pragma unroll
;           for (int j = 0; j < 8; ++j) bw[ks][hf][j] = (_Float16)rwp[(32 * ks + j) * 32 + 16 * hf]; }
	v_cvt_pk_f16_f32 v8, v8, v74
	v_cvt_pk_f16_f32 v9, v9, v75
	v_cvt_pk_f16_f32 v10, v10, v76
	v_cvt_pk_f16_f32 v11, v11, v77
	v_cvt_pk_f16_f32 v12, v12, v78
	v_cvt_pk_f16_f32 v13, v13, v79
	v_cvt_pk_f16_f32 v14, v14, v84
	v_cvt_pk_f16_f32 v15, v15, v85
	global_load_dword v32, v[140:141], off
	global_load_dword v104, v[140:141], off offset:128
	global_load_dword v33, v[140:141], off offset:256
	global_load_dword v105, v[140:141], off offset:384
	global_load_dword v34, v[140:141], off offset:512
	global_load_dword v106, v[140:141], off offset:640
	global_load_dword v35, v[140:141], off offset:768
	global_load_dword v107, v[140:141], off offset:896
	global_load_dword v36, v[140:141], off offset:64
	global_load_dword v108, v[140:141], off offset:192
	global_load_dword v37, v[140:141], off offset:320
	global_load_dword v109, v[140:141], off offset:448
	global_load_dword v38, v[140:141], off offset:576
	global_load_dword v110, v[140:141], off offset:704
	global_load_dword v39, v[140:141], off offset:832
	global_load_dword v111, v[140:141], off offset:960
	s_waitcnt vmcnt(32)
	v_cvt_pk_f16_f32 v16, v16, v86
	v_cvt_pk_f16_f32 v17, v17, v87
	v_cvt_pk_f16_f32 v18, v18, v88
	v_cvt_pk_f16_f32 v19, v19, v89
	v_cvt_pk_f16_f32 v20, v20, v90
	v_cvt_pk_f16_f32 v21, v21, v91
	v_cvt_pk_f16_f32 v22, v22, v92
	v_cvt_pk_f16_f32 v23, v23, v93
	global_load_dword v40, v[142:143], off offset:-4096
	global_load_dword v112, v[142:143], off offset:-3968
	global_load_dword v41, v[142:143], off offset:-3840
	global_load_dword v113, v[142:143], off offset:-3712
	global_load_dword v42, v[142:143], off offset:-3584
	global_load_dword v114, v[142:143], off offset:-3456
	global_load_dword v43, v[142:143], off offset:-3328
	global_load_dword v115, v[142:143], off offset:-3200
	global_load_dword v44, v[142:143], off offset:-4032
	global_load_dword v116, v[142:143], off offset:-3904
	global_load_dword v45, v[142:143], off offset:-3776
	global_load_dword v117, v[142:143], off offset:-3648
	global_load_dword v46, v[142:143], off offset:-3520
	global_load_dword v118, v[142:143], off offset:-3392
	global_load_dword v47, v[142:143], off offset:-3264
	global_load_dword v119, v[142:143], off offset:-3136
	s_waitcnt vmcnt(32)
	v_cvt_pk_f16_f32 v24, v24, v94
	v_cvt_pk_f16_f32 v25, v25, v95
	v_cvt_pk_f16_f32 v26, v26, v96
	v_cvt_pk_f16_f32 v27, v27, v97
	v_cvt_pk_f16_f32 v28, v28, v98
	v_cvt_pk_f16_f32 v29, v29, v99
	v_cvt_pk_f16_f32 v30, v30, v102
	v_cvt_pk_f16_f32 v31, v31, v103
	global_load_dword v48, v[142:143], off
	global_load_dword v120, v[142:143], off offset:128
	global_load_dword v49, v[142:143], off offset:256
	global_load_dword v121, v[142:143], off offset:384
	global_load_dword v50, v[142:143], off offset:512
	global_load_dword v122, v[142:143], off offset:640
	global_load_dword v51, v[142:143], off offset:768
	global_load_dword v123, v[142:143], off offset:896
	global_load_dword v52, v[142:143], off offset:64
	global_load_dword v124, v[142:143], off offset:192
	global_load_dword v53, v[142:143], off offset:320
	global_load_dword v125, v[142:143], off offset:448
	global_load_dword v54, v[142:143], off offset:576
	global_load_dword v128, v[142:143], off offset:704
	global_load_dword v55, v[142:143], off offset:832
	global_load_dword v129, v[142:143], off offset:960
	s_waitcnt vmcnt(32)
; template <bool RES_F32> ...
;     ...
;     { const float* rwp = rw + (size_t)(256 * wid + 8 * (lane >> 4)) * 32 + (lane & 15);
; #pragma unroll
;       for (int ks = 0; ks < 8; ++ks)
; #pragma unroll
;         for (int hf = 0; hf < 2; ++hf)
; #pragma unroll
;           for (int j = 0; j < 8; ++j) bw[ks][hf][j] = (_Float16)rwp[(32 * ks + j) * 32 + 16 * hf]; }
;     typedef typename std::conditional<RES_F32, f32x4, u32x2>::type res_t;
;     typedef typename std::conditional<F8_MIX != 0, unsigned, u32x2>::type mix_t;
;     mix_t mv[2][8]; res_t rv[2][8];
;     ...
;     const int ntile = T_ / 16;
;     int ntl = 0;
;     if (bid < ntile) LNR_LOAD(bid, 0);
	v_cvt_pk_f16_f32 v32, v32, v104
	v_cvt_pk_f16_f32 v33, v33, v105
	v_cvt_pk_f16_f32 v34, v34, v106
	v_cvt_pk_f16_f32 v35, v35, v107
	v_cvt_pk_f16_f32 v36, v36, v108
	v_cvt_pk_f16_f32 v37, v37, v109
	v_cvt_pk_f16_f32 v38, v38, v110
	v_cvt_pk_f16_f32 v39, v39, v111
	global_load_dword v56, v[144:145], off offset:-4096
	global_load_dword v130, v[144:145], off offset:-3968
	global_load_dword v57, v[144:145], off offset:-3840
	global_load_dword v131, v[144:145], off offset:-3712
	global_load_dword v58, v[144:145], off offset:-3584
	global_load_dword v132, v[144:145], off offset:-3456
	global_load_dword v59, v[144:145], off offset:-3328
	global_load_dword v133, v[144:145], off offset:-3200
	global_load_dword v60, v[144:145], off offset:-4032
	global_load_dword v134, v[144:145], off offset:-3904
	global_load_dword v61, v[144:145], off offset:-3776
	global_load_dword v135, v[144:145], off offset:-3648
	global_load_dword v62, v[144:145], off offset:-3520
	global_load_dword v136, v[144:145], off offset:-3392
	global_load_dword v63, v[144:145], off offset:-3264
	global_load_dword v137, v[144:145], off offset:-3136
	s_waitcnt vmcnt(32)
	v_cvt_pk_f16_f32 v40, v40, v112
	v_cvt_pk_f16_f32 v41, v41, v113
	v_cvt_pk_f16_f32 v42, v42, v114
	v_cvt_pk_f16_f32 v43, v43, v115
	v_cvt_pk_f16_f32 v44, v44, v116
	v_cvt_pk_f16_f32 v45, v45, v117
	v_cvt_pk_f16_f32 v46, v46, v118
	v_cvt_pk_f16_f32 v47, v47, v119
	s_waitcnt vmcnt(16)
	v_cvt_pk_f16_f32 v48, v48, v120
	v_cvt_pk_f16_f32 v49, v49, v121
	v_cvt_pk_f16_f32 v50, v50, v122
	v_cvt_pk_f16_f32 v51, v51, v123
	v_cvt_pk_f16_f32 v52, v52, v124
	v_cvt_pk_f16_f32 v53, v53, v125
	v_cvt_pk_f16_f32 v54, v54, v128
	v_cvt_pk_f16_f32 v55, v55, v129
	s_waitcnt vmcnt(0)
	v_cvt_pk_f16_f32 v56, v56, v130
	v_cvt_pk_f16_f32 v57, v57, v131
	v_cvt_pk_f16_f32 v58, v58, v132
	v_cvt_pk_f16_f32 v59, v59, v133
	v_cvt_pk_f16_f32 v60, v60, v134
	v_cvt_pk_f16_f32 v61, v61, v135
	v_cvt_pk_f16_f32 v62, v62, v136
	v_cvt_pk_f16_f32 v63, v63, v137
	v_lshl_or_b32 v66, v81, 2, s1
	v_lshl_add_u64 v[68:69], s[96:97], 0, v[66:67]
	v_lshl_add_u64 v[66:67], v[66:67], 1, s[76:77]
	global_load_dword v161, v[68:69], off
	global_load_dwordx2 v[84:85], v[66:67], off
	global_load_dword v162, v[68:69], off offset:256
	global_load_dwordx2 v[86:87], v[66:67], off offset:512
	global_load_dword v163, v[68:69], off offset:512
	global_load_dwordx2 v[88:89], v[66:67], off offset:1024
	global_load_dword v164, v[68:69], off offset:768
	global_load_dwordx2 v[90:91], v[66:67], off offset:1536
	global_load_dword v165, v[68:69], off offset:1024
	global_load_dwordx2 v[92:93], v[66:67], off offset:2048
	global_load_dword v166, v[68:69], off offset:1280
	global_load_dwordx2 v[94:95], v[66:67], off offset:2560
	global_load_dword v167, v[68:69], off offset:1536
	global_load_dwordx2 v[96:97], v[66:67], off offset:3072
	global_load_dword v168, v[68:69], off offset:1792
	global_load_dwordx2 v[98:99], v[66:67], off offset:3584
	s_lshl_b32 s1, s0, 10
	v_and_b32_e32 v65, 0x3fffffe0, v80
	v_lshlrev_b32_e32 v66, 2, v64
	s_add_i32 s57, s1, 0
	s_lshl_b32 s1, s0, 11
	v_lshlrev_b32_e32 v65, 2, v65
	v_and_b32_e32 v232, 0x7c, v66
	s_mulk_i32 s0, 0x3c20
	s_add_i32 s58, s2, s1
	v_add3_u32 v169, s2, v65, v232
	v_lshlrev_b32_e32 v65, 2, v80
	v_readlane_b32 s1, v254, 56
	s_add_i32 s59, s57, s0
	s_mul_i32 s0, s60, 0x2010
	v_add_u32_e32 v170, s1, v65
	v_readlane_b32 s1, v254, 57
	s_add_i32 s62, s0, 0
	v_readlane_b32 s0, v254, 27
	v_add_u32_e32 v171, s1, v65
	v_lshlrev_b32_e32 v65, 7, v80
	s_movk_i32 s1, 0x7c
	v_lshl_add_u32 v104, v64, 1, s0
	v_readlane_b32 s0, v254, 28
	v_mul_lo_u32 v66, v80, s1
	v_lshl_add_u64 v[102:103], s[42:43], 0, v[232:233]
	v_lshl_add_u32 v174, v64, 3, s0
	v_add_u32_e32 v64, 0, v65
	v_add_u32_e32 v172, v171, v66
	v_add_u32_e32 v173, v170, v66
	v_add_u32_e32 v175, 0x24a00, v64
	s_mov_b32 s2, s30
	s_branch .LBB0_772

; #define LAS __attribute__((address_space(3)))
; template <bool RES_F32> ...
;     const int wid = __builtin_amdgcn_readfirstlane(tid >> 6), lane = tid & 63;
;     float ALPHA = 1.4142135623730951f; asm volatile("" : "+v"(ALPHA));
;     LAS float* xs = (LAS float*)lds; LAS float* part = (LAS float*)(lds + LNR_PART); LAS float* scs = (LAS float*)(lds + LNR_SC); LAS float* sels = (LAS float*)(lds + LNR_SEL);
;     LAS int* ble = (LAS int*)(lds + LNR_BLE); LAS int* hist = (LAS int*)(lds + LNR_HIST);
;     f16x8 bw[8][2];
;     { const float* rwp = rw + (size_t)(256 * wid + 8 * (lane >> 4)) * 32 + (lane & 15);
; #pragma unroll
;       for (int ks = 0; ks < 8; ++ks)
; #pragma unroll
;         for (int hf = 0; hf < 2; ++hf)
; #pragma unroll
;           for (int j = 0; j < 8; ++j) bw[ks][hf][j] = (_Float16)rwp[(32 * ks + j) * 32 + 16 * hf]; }
;     typedef typename std::conditional<RES_F32, f32x4, u32x2>::type res_t;
;     typedef typename std::conditional<F8_MIX != 0, unsigned, u32x2>::type mix_t;
;     mix_t mv[2][8]; res_t rv[2][8];
;     ...
;     const int ntile = T_ / 16;
;     int ntl = 0;
;     if (bid < ntile) LNR_LOAD(bid, 0);
.LBB0_807:
	s_and_b64 vcc, exec, s[0:1]
	s_cbranch_vccz .LBB0_846
	v_readlane_b32 s2, v253, 26
	v_mbcnt_lo_u32_b32 v96, -1, 0
	v_mbcnt_hi_u32_b32 v96, -1, v96
	v_readlane_b32 s3, v253, 27
	v_add_u32_e32 v144, s5, v96
	v_mov_b32_e32 v146, 0x3fb504f3
	v_readfirstlane_b32 s0, v144
	s_andn2_b64 vcc, exec, s[2:3]
	s_mov_b32 s56, 0
	s_cbranch_vccnz .LBB0_815
	s_add_u32 s57, s70, 0x3a600000
	v_lshrrev_b32_e32 v0, 1, v96
	s_addc_u32 s58, s71, 0
	s_ashr_i32 s0, s0, 6
	v_and_b32_e32 v0, 24, v0
	s_load_dwordx4 s[72:75], s[64:65], 0x0
	s_load_dwordx2 s[2:3], s[64:65], 0x10
	s_load_dwordx4 s[76:79], s[64:65], 0x38
	v_lshl_or_b32 v0, s0, 8, v0
	s_waitcnt vmcnt(0)
	v_ashrrev_i32_e32 v1, 31, v0
	v_lshlrev_b64 v[0:1], 7, v[0:1]
	v_and_b32_e32 v2, 15, v96
	s_waitcnt lgkmcnt(0)
	v_lshl_add_u64 v[0:1], s[74:75], 0, v[0:1]
	v_lshlrev_b32_e32 v232, 2, v2
	v_lshl_add_u64 v[56:57], v[0:1], 0, v[232:233]
	s_lshl_b32 s68, s0, 1
	s_ashr_i32 s69, s68, 31
	s_lshl_b64 s[70:71], s[68:69], 11
	v_readlane_b32 s6, v253, 44
	v_readlane_b32 s7, v253, 45
	v_and_b32_e32 v145, 63, v96
	v_and_b32_e32 v97, 0x3fffffe0, v144
	v_lshlrev_b32_e32 v98, 2, v96
	v_lshlrev_b32_e32 v97, 2, v97
	v_and_b32_e32 v232, 0x7c, v98
	v_mov_b32_e32 v147, v146
	v_mov_b32_e32 v148, v146
	v_mov_b32_e32 v149, v146
	v_lshl_add_u64 v[150:151], s[2:3], 0, v[232:233]
	v_cmp_gt_i32_e64 s[38:39], 16, v144
	s_mov_b32 s2, s30
	s_add_u32 s1, s70, s6
	s_addc_u32 s6, s71, s7
	s_or_b32 s62, s68, 1
	s_ashr_i32 s63, s62, 31
	v_add_co_u32_e32 v132, vcc, 0x2000, v56
	s_nop 1
	v_addc_co_u32_e32 v133, vcc, 0, v57, vcc
	v_add_co_u32_e32 v134, vcc, 0x4000, v56
	s_nop 1
	v_addc_co_u32_e32 v135, vcc, 0, v57, vcc
	v_add_co_u32_e32 v136, vcc, 0x6000, v56
	s_nop 1
	v_addc_co_u32_e32 v137, vcc, 0, v57, vcc
	v_add_co_u32_e32 v138, vcc, 0x8000, v56
	s_nop 1
	v_addc_co_u32_e32 v139, vcc, 0, v57, vcc
	global_load_dword v0, v[56:57], off
	global_load_dword v64, v[56:57], off offset:128
	global_load_dword v1, v[56:57], off offset:256
	global_load_dword v65, v[56:57], off offset:384
	global_load_dword v2, v[56:57], off offset:512
	global_load_dword v66, v[56:57], off offset:640
	global_load_dword v3, v[56:57], off offset:768
	global_load_dword v67, v[56:57], off offset:896
	global_load_dword v4, v[56:57], off offset:64
	global_load_dword v68, v[56:57], off offset:192
	global_load_dword v5, v[56:57], off offset:320
	global_load_dword v69, v[56:57], off offset:448
	global_load_dword v6, v[56:57], off offset:576
	global_load_dword v70, v[56:57], off offset:704
	global_load_dword v7, v[56:57], off offset:832
	global_load_dword v71, v[56:57], off offset:960
	global_load_dword v8, v[132:133], off offset:-4096
	global_load_dword v72, v[132:133], off offset:-3968
	global_load_dword v9, v[132:133], off offset:-3840
	global_load_dword v73, v[132:133], off offset:-3712
	global_load_dword v10, v[132:133], off offset:-3584
	global_load_dword v74, v[132:133], off offset:-3456
	global_load_dword v11, v[132:133], off offset:-3328
	global_load_dword v75, v[132:133], off offset:-3200
	global_load_dword v12, v[132:133], off offset:-4032
	global_load_dword v76, v[132:133], off offset:-3904
	global_load_dword v13, v[132:133], off offset:-3776
	global_load_dword v77, v[132:133], off offset:-3648
	global_load_dword v14, v[132:133], off offset:-3520
	global_load_dword v78, v[132:133], off offset:-3392
	global_load_dword v15, v[132:133], off offset:-3264
	global_load_dword v79, v[132:133], off offset:-3136
	global_load_dword v16, v[132:133], off
	global_load_dword v80, v[132:133], off offset:128
	global_load_dword v17, v[132:133], off offset:256
	global_load_dword v81, v[132:133], off offset:384
	global_load_dword v18, v[132:133], off offset:512
	global_load_dword v82, v[132:133], off offset:640
	global_load_dword v19, v[132:133], off offset:768
	global_load_dword v83, v[132:133], off offset:896
	global_load_dword v20, v[132:133], off offset:64
	global_load_dword v84, v[132:133], off offset:192
	global_load_dword v21, v[132:133], off offset:320
	global_load_dword v85, v[132:133], off offset:448
	global_load_dword v22, v[132:133], off offset:576
	global_load_dword v86, v[132:133], off offset:704
	global_load_dword v23, v[132:133], off offset:832
	global_load_dword v87, v[132:133], off offset:960
	s_waitcnt vmcnt(32)
	v_cvt_pk_f16_f32 v0, v0, v64
	v_cvt_pk_f16_f32 v1, v1, v65
	v_cvt_pk_f16_f32 v2, v2, v66
	v_cvt_pk_f16_f32 v3, v3, v67
	v_cvt_pk_f16_f32 v4, v4, v68
	v_cvt_pk_f16_f32 v5, v5, v69
	v_cvt_pk_f16_f32 v6, v6, v70
	v_cvt_pk_f16_f32 v7, v7, v71
	global_load_dword v24, v[134:135], off offset:-4096
	global_load_dword v88, v[134:135], off offset:-3968
	global_load_dword v25, v[134:135], off offset:-3840
	global_load_dword v89, v[134:135], off offset:-3712
	global_load_dword v26, v[134:135], off offset:-3584
	global_load_dword v90, v[134:135], off offset:-3456
	global_load_dword v27, v[134:135], off offset:-3328
	global_load_dword v91, v[134:135], off offset:-3200
	global_load_dword v28, v[134:135], off offset:-4032
	global_load_dword v92, v[134:135], off offset:-3904
	global_load_dword v29, v[134:135], off offset:-3776
	global_load_dword v93, v[134:135], off offset:-3648
	global_load_dword v30, v[134:135], off offset:-3520
	global_load_dword v94, v[134:135], off offset:-3392
	global_load_dword v31, v[134:135], off offset:-3264
	global_load_dword v95, v[134:135], off offset:-3136
	s_waitcnt vmcnt(32)
; template <bool RES_F32> ...
;     ...
;     { const float* rwp = rw + (size_t)(256 * wid + 8 * (lane >> 4)) * 32 + (lane & 15);
; #pragma unroll
;       for (int ks = 0; ks < 8; ++ks)
; #pragma unroll
;         for (int hf = 0; hf < 2; ++hf)
; #pragma unroll
;           for (int j = 0; j < 8; ++j) bw[ks][hf][j] = (_Float16)rwp[(32 * ks + j) * 32 + 16 * hf]; }
	v_cvt_pk_f16_f32 v8, v8, v72
	v_cvt_pk_f16_f32 v9, v9, v73
	v_cvt_pk_f16_f32 v10, v10, v74
	v_cvt_pk_f16_f32 v11, v11, v75
	v_cvt_pk_f16_f32 v12, v12, v76
	v_cvt_pk_f16_f32 v13, v13, v77
	v_cvt_pk_f16_f32 v14, v14, v78
	v_cvt_pk_f16_f32 v15, v15, v79
	global_load_dword v32, v[134:135], off
	global_load_dword v100, v[134:135], off offset:128
	global_load_dword v33, v[134:135], off offset:256
	global_load_dword v101, v[134:135], off offset:384
	global_load_dword v34, v[134:135], off offset:512
	global_load_dword v102, v[134:135], off offset:640
	global_load_dword v35, v[134:135], off offset:768
	global_load_dword v103, v[134:135], off offset:896
	global_load_dword v36, v[134:135], off offset:64
	global_load_dword v104, v[134:135], off offset:192
	global_load_dword v37, v[134:135], off offset:320
	global_load_dword v105, v[134:135], off offset:448
	global_load_dword v38, v[134:135], off offset:576
	global_load_dword v106, v[134:135], off offset:704
	global_load_dword v39, v[134:135], off offset:832
	global_load_dword v107, v[134:135], off offset:960
	s_waitcnt vmcnt(32)
	v_cvt_pk_f16_f32 v16, v16, v80
	v_cvt_pk_f16_f32 v17, v17, v81
	v_cvt_pk_f16_f32 v18, v18, v82
	v_cvt_pk_f16_f32 v19, v19, v83
	v_cvt_pk_f16_f32 v20, v20, v84
	v_cvt_pk_f16_f32 v21, v21, v85
	v_cvt_pk_f16_f32 v22, v22, v86
	v_cvt_pk_f16_f32 v23, v23, v87
	global_load_dword v40, v[136:137], off offset:-4096
	global_load_dword v108, v[136:137], off offset:-3968
	global_load_dword v41, v[136:137], off offset:-3840
	global_load_dword v109, v[136:137], off offset:-3712
	global_load_dword v42, v[136:137], off offset:-3584
	global_load_dword v110, v[136:137], off offset:-3456
	global_load_dword v43, v[136:137], off offset:-3328
	global_load_dword v111, v[136:137], off offset:-3200
	global_load_dword v44, v[136:137], off offset:-4032
	global_load_dword v112, v[136:137], off offset:-3904
	global_load_dword v45, v[136:137], off offset:-3776
	global_load_dword v113, v[136:137], off offset:-3648
	global_load_dword v46, v[136:137], off offset:-3520
	global_load_dword v114, v[136:137], off offset:-3392
	global_load_dword v47, v[136:137], off offset:-3264
	global_load_dword v115, v[136:137], off offset:-3136
	s_waitcnt vmcnt(32)
	v_cvt_pk_f16_f32 v24, v24, v88
	v_cvt_pk_f16_f32 v25, v25, v89
	v_cvt_pk_f16_f32 v26, v26, v90
	v_cvt_pk_f16_f32 v27, v27, v91
	v_cvt_pk_f16_f32 v28, v28, v92
	v_cvt_pk_f16_f32 v29, v29, v93
	v_cvt_pk_f16_f32 v30, v30, v94
	v_cvt_pk_f16_f32 v31, v31, v95
	global_load_dword v48, v[136:137], off
	global_load_dword v116, v[136:137], off offset:128
	global_load_dword v49, v[136:137], off offset:256
	global_load_dword v117, v[136:137], off offset:384
	global_load_dword v50, v[136:137], off offset:512
	global_load_dword v118, v[136:137], off offset:640
	global_load_dword v51, v[136:137], off offset:768
	global_load_dword v119, v[136:137], off offset:896
	global_load_dword v52, v[136:137], off offset:64
	global_load_dword v120, v[136:137], off offset:192
	global_load_dword v53, v[136:137], off offset:320
	global_load_dword v121, v[136:137], off offset:448
	global_load_dword v54, v[136:137], off offset:576
	global_load_dword v122, v[136:137], off offset:704
	global_load_dword v55, v[136:137], off offset:832
	global_load_dword v123, v[136:137], off offset:960
	s_waitcnt vmcnt(32)
; template <bool RES_F32> ...
;     ...
;     { const float* rwp = rw + (size_t)(256 * wid + 8 * (lane >> 4)) * 32 + (lane & 15);
; #pragma unroll
;       for (int ks = 0; ks < 8; ++ks)
; #pragma unroll
;         for (int hf = 0; hf < 2; ++hf)
; #pragma unroll
;           for (int j = 0; j < 8; ++j) bw[ks][hf][j] = (_Float16)rwp[(32 * ks + j) * 32 + 16 * hf]; }
;     typedef typename std::conditional<RES_F32, f32x4, u32x2>::type res_t;
;     typedef typename std::conditional<F8_MIX != 0, unsigned, u32x2>::type mix_t;
;     mix_t mv[2][8]; res_t rv[2][8];
;     ...
;     const int ntile = T_ / 16;
;     int ntl = 0;
;     if (bid < ntile) LNR_LOAD(bid, 0);
	v_cvt_pk_f16_f32 v32, v32, v100
	v_cvt_pk_f16_f32 v33, v33, v101
	v_cvt_pk_f16_f32 v34, v34, v102
	v_cvt_pk_f16_f32 v35, v35, v103
	v_cvt_pk_f16_f32 v36, v36, v104
	v_cvt_pk_f16_f32 v37, v37, v105
	v_cvt_pk_f16_f32 v38, v38, v106
	v_cvt_pk_f16_f32 v39, v39, v107
	global_load_dword v56, v[138:139], off offset:-4096
	global_load_dword v124, v[138:139], off offset:-3968
	global_load_dword v57, v[138:139], off offset:-3840
	global_load_dword v125, v[138:139], off offset:-3712
	global_load_dword v58, v[138:139], off offset:-3584
	global_load_dword v126, v[138:139], off offset:-3456
	global_load_dword v59, v[138:139], off offset:-3328
	global_load_dword v127, v[138:139], off offset:-3200
	global_load_dword v60, v[138:139], off offset:-4032
	global_load_dword v128, v[138:139], off offset:-3904
	global_load_dword v61, v[138:139], off offset:-3776
	global_load_dword v129, v[138:139], off offset:-3648
	global_load_dword v62, v[138:139], off offset:-3520
	global_load_dword v130, v[138:139], off offset:-3392
	global_load_dword v63, v[138:139], off offset:-3264
	global_load_dword v131, v[138:139], off offset:-3136
	s_waitcnt vmcnt(32)
	v_cvt_pk_f16_f32 v40, v40, v108
	v_cvt_pk_f16_f32 v41, v41, v109
	v_cvt_pk_f16_f32 v42, v42, v110
	v_cvt_pk_f16_f32 v43, v43, v111
	v_cvt_pk_f16_f32 v44, v44, v112
	v_cvt_pk_f16_f32 v45, v45, v113
	v_cvt_pk_f16_f32 v46, v46, v114
	v_cvt_pk_f16_f32 v47, v47, v115
	s_waitcnt vmcnt(16)
	v_cvt_pk_f16_f32 v48, v48, v116
	v_cvt_pk_f16_f32 v49, v49, v117
	v_cvt_pk_f16_f32 v50, v50, v118
	v_cvt_pk_f16_f32 v51, v51, v119
	v_cvt_pk_f16_f32 v52, v52, v120
	v_cvt_pk_f16_f32 v53, v53, v121
	v_cvt_pk_f16_f32 v54, v54, v122
	v_cvt_pk_f16_f32 v55, v55, v123
	s_waitcnt vmcnt(0)
	v_cvt_pk_f16_f32 v56, v56, v124
	v_cvt_pk_f16_f32 v57, v57, v125
	v_cvt_pk_f16_f32 v58, v58, v126
	v_cvt_pk_f16_f32 v59, v59, v127
	v_cvt_pk_f16_f32 v60, v60, v128
	v_cvt_pk_f16_f32 v61, v61, v129
	v_cvt_pk_f16_f32 v62, v62, v130
	v_cvt_pk_f16_f32 v63, v63, v131
	v_lshl_or_b32 v64, v145, 2, s1
	v_mov_b32_e32 v65, s6
	v_lshl_add_u64 v[92:93], s[96:97], 0, v[64:65]
	v_lshl_add_u64 v[80:81], v[64:65], 2, s[72:73]
	global_load_dword v193, v[92:93], off
	global_load_dwordx4 v[64:67], v[80:81], off
	global_load_dword v194, v[92:93], off offset:256
	global_load_dwordx4 v[68:71], v[80:81], off offset:1024
	global_load_dword v195, v[92:93], off offset:512
	global_load_dwordx4 v[72:75], v[80:81], off offset:2048
	global_load_dword v196, v[92:93], off offset:768
	global_load_dwordx4 v[76:79], v[80:81], off offset:3072
	global_load_dword v197, v[92:93], off offset:1024
	v_add_co_u32_e32 v94, vcc, s90, v80
	s_lshl_b32 s1, s0, 10
	s_nop 0
	v_addc_co_u32_e32 v95, vcc, 0, v81, vcc
	global_load_dwordx4 v[80:83], v[94:95], off
	global_load_dword v198, v[92:93], off offset:1280
	global_load_dwordx4 v[84:87], v[94:95], off offset:1024
	global_load_dword v199, v[92:93], off offset:1536
	global_load_dwordx4 v[88:91], v[94:95], off offset:2048
	global_load_dword v200, v[92:93], off offset:1792
	s_nop 0
	global_load_dwordx4 v[92:95], v[94:95], off offset:3072
	s_add_i32 s59, s1, 0
	s_lshl_b32 s1, s0, 11
	v_readlane_b32 s6, v254, 55
	s_mulk_i32 s0, 0x3c20
	s_add_i32 s60, s6, s1
	v_add3_u32 v201, s6, v97, v232
	v_lshlrev_b32_e32 v97, 2, v144
	v_readlane_b32 s1, v254, 56
	s_add_i32 s61, s59, s0
	s_mul_i32 s0, s62, 0x2010
	v_add_u32_e32 v202, s1, v97
	v_readlane_b32 s1, v254, 57
	s_add_i32 s64, s0, 0
	v_readlane_b32 s0, v254, 27
	v_add_u32_e32 v203, s1, v97
	v_lshlrev_b32_e32 v97, 7, v144
	s_movk_i32 s1, 0x7c
	v_lshl_add_u32 v152, v96, 1, s0
	v_readlane_b32 s0, v254, 28
	v_mul_lo_u32 v98, v144, s1
	v_add_u32_e32 v204, v203, v98
	v_lshl_add_u32 v206, v96, 3, s0
	v_add_u32_e32 v96, 0, v97
	v_add_u32_e32 v205, v202, v98
	v_add_u32_e32 v207, 0x24a00, v96
	s_branch .LBB0_811
